# as previous plus P0 wide int8 weight stores write-through (sc1)
# speedup vs baseline: 1.0383x; 1.0052x over previous
; #define P0_LOAD(T, V) do { _Pragma("unroll") for (int i = 0; i < 8; ++i) V[i] = *(const GAS f32x4*)(T.src + (size_t)(i * 8 + (F.lane >> 3)) * T.N + (F.lane & 7) * 4); } while (0)
; __device__ __forceinline__ void p0_prologue(Frame& F) {
;     ...
;     {
;         int it = gw; TItem ta, tb; f32x4 va[8], vb[8];
;         if (it < NITEMS) {
;             ta = decode(it); P0_LOAD(ta, va);
;             for (;;) {
;                 { const int itn = it + NGW; tb = decode(itn < NITEMS ? itn : gw); P0_LOAD(tb, vb); }
;                 P0_PROC(ta, va); it += NGW; if (it >= NITEMS) break;
;                 { const int itn = it + NGW; ta = decode(itn < NITEMS ? itn : gw); P0_LOAD(ta, va); }
;                 P0_PROC(tb, vb); it += NGW; if (it >= NITEMS) break;
.LBB0_29:
	v_lshl_add_u64 v[40:41], s[26:27], 0, v[40:41]
	v_mul_hi_i32_i24_e32 v39, s28, v38
	v_mul_i32_i24_e32 v38, s28, v38
	v_lshl_add_u64 v[38:39], v[40:41], 0, v[38:39]
	global_store_dwordx4 v[38:39], v[34:37], off sc1
	s_waitcnt lgkmcnt(0)
	s_add_i32 s71, s68, s33
	s_cmp_gt_i32 s71, 0xdfff
	s_cselect_b64 s[36:37], -1, 0

.LBB0_54:
	ds_read2_b32 v[8:9], v75 offset0:16 offset1:49
	v_lshl_add_u64 v[6:7], s[0:1], 0, v[78:79]
	v_mad_u64_u32 v[6:7], s[38:39], v82, s40, v[6:7]
	global_store_dwordx4 v[6:7], v[2:5], off sc1
	s_waitcnt lgkmcnt(0)
	v_mul_f32_e32 v7, s41, v8
	v_mul_f32_e32 v6, s41, v9
	s_andn2_b64 vcc, exec, s[36:37]
	s_mov_b64 s[36:37], -1
	s_cbranch_vccnz .LBB0_56
	ds_read2_b32 v[4:5], v75 offset0:82 offset1:115
	ds_read2_b32 v[8:9], v75 offset0:148 offset1:181
	v_mov_b32_e32 v2, v71
	v_mov_b32_e32 v3, v71
	v_add_u32_e32 v12, 0x400, v75
	s_waitcnt lgkmcnt(1)
	v_mul_f32_e32 v10, s41, v4
	v_mul_f32_e32 v11, s41, v5
	s_waitcnt lgkmcnt(0)
	v_mul_f32_e32 v8, s41, v8
	v_mul_f32_e32 v9, s41, v9
	ds_read2_b32 v[4:5], v75 offset0:214 offset1:247
	v_cvt_pk_fp8_f32 v2, v7, v6
	v_cvt_pk_fp8_f32 v3, v8, v9
	ds_read2_b32 v[8:9], v12 offset0:24 offset1:57
	s_mov_b64 s[36:37], 0
	v_cvt_pk_fp8_f32 v2, v10, v11 op_sel:[0,0,1]
	s_waitcnt lgkmcnt(1)
	v_mul_f32_e32 v4, s41, v4
	v_mul_f32_e32 v5, s41, v5
	ds_read2_b32 v[10:11], v12 offset0:90 offset1:123
	v_cvt_pk_fp8_f32 v3, v4, v5 op_sel:[0,0,1]
	s_waitcnt lgkmcnt(1)
	v_mul_f32_e32 v5, s41, v8
	v_mul_f32_e32 v13, s41, v9
	ds_read2_b32 v[8:9], v12 offset0:156 offset1:189
	v_mov_b32_e32 v4, v71
	v_cvt_pk_fp8_f32 v4, v5, v13
	s_waitcnt lgkmcnt(1)
	v_mul_f32_e32 v13, s41, v10
	v_mul_f32_e32 v14, s41, v11
	ds_read2_b32 v[10:11], v12 offset0:222 offset1:255
	s_waitcnt lgkmcnt(1)
	v_mul_f32_e32 v8, s41, v8
	v_mul_f32_e32 v9, s41, v9
	v_mov_b32_e32 v5, v71
	v_cvt_pk_fp8_f32 v5, v8, v9
	s_waitcnt lgkmcnt(0)
	v_mul_f32_e32 v8, s41, v10
	v_mul_f32_e32 v9, s41, v11
	v_cvt_pk_fp8_f32 v4, v13, v14 op_sel:[0,0,1]
	v_cvt_pk_fp8_f32 v5, v8, v9 op_sel:[0,0,1]

; __device__ __forceinline__ void p0_prologue(Frame& F) {
;     ...
;     auto decode = [&](int it) { TItem t; int r = it;
;         if (r < I_1) { const int kb = P0_KB(r, INC / 32), nb = P0_NB(r, INC / 32); t.src = F.in[I_WIN] + (size_t)(64 * kb) * INC + 32 * nb; t.N = INC;
;             if (nb < Z8_COL0 / 32) { t.fp8 = 0; t.ldo = 2 * LDP; t.dst = (unsigned char*)WINT + (size_t)(32 * nb) * (2 * LDP) + 2 * 64 * kb; t.sc = 1.f; }
;             else { t.fp8 = LOWP; t.ldo = 2 * LDP8; t.dst = (unsigned char*)(F.ws + WS_WIN8) + (size_t)(32 * nb - Z8_COL0) * (2 * LDP8) + 64 * kb; t.sc = WIN8_SCALE; }
;             return t; } r -= I_1;
;         if (r < I_2) { const int kb = P0_KB(r, DM / 32), nb = P0_NB(r, DM / 32); t.src = F.in[I_WCO] + (size_t)(64 * kb) * DM + 32 * nb; t.N = DM;
;             if (GEMM2_FUSED) { t.fp8 = 1; t.ldo = 2 * LDP8; t.dst = (unsigned char*)(F.ws + WS_WC) + (size_t)(32 * nb) * (2 * LDP8) + 64 * kb; t.sc = WCO8_SCALE; }
;             else if (CONVOUT_INT8 || CONVOUT_FP8) { t.fp8 = CONVOUT_FP8 ? 1 : 2; t.ldo = 2 * LDH8; t.dst = (unsigned char*)WCOT + (size_t)(32 * nb) * (2 * LDH8) + 64 * kb; t.sc = WCO8_SCALE; }
;             else { t.fp8 = 0; t.ldo = 2 * LDH; t.dst = (unsigned char*)WCOT + (size_t)(32 * nb) * (2 * LDH) + 2 * 64 * kb; t.sc = 1.f; }
;             return t; } r -= I_2;
;         if (r < I_3) { const int kb = P0_KB(r, DM / 32), nb = P0_NB(r, DM / 32); t.src = F.in[I_WAO] + (size_t)(64 * kb) * DM + 32 * nb; t.N = DM; t.fp8 = 1; t.sc = WAO8_SCALE;
;             if (GEMM2_FUSED) { t.ldo = 2 * LDP8; t.dst = (unsigned char*)(F.ws + WS_WC) + (size_t)(32 * nb) * (2 * LDP8) + 2048 + 64 * kb; }
;             else { t.ldo = 2 * LDH8; t.dst = (unsigned char*)(F.ws + WS_WAO8) + (size_t)(32 * nb) * (2 * LDH8) + 64 * kb; }
;             return t; } r -= I_3;
;     ...
;     {
;         int it = gw; TItem ta, tb; f32x4 va[8], vb[8];
;         if (it < NITEMS) {
;             ta = decode(it); P0_LOAD(ta, va);
;             for (;;) {
;                 { const int itn = it + NGW; tb = decode(itn < NITEMS ? itn : gw); P0_LOAD(tb, vb); }
;                 P0_PROC(ta, va); it += NGW; if (it >= NITEMS) break;
;                 { const int itn = it + NGW; ta = decode(itn < NITEMS ? itn : gw); P0_LOAD(ta, va); }
;                 P0_PROC(tb, vb); it += NGW; if (it >= NITEMS) break;
.LBB0_59:
	ds_read2_b32 v[6:7], v77 offset1:8
	ds_read2_b32 v[8:9], v77 offset0:33 offset1:41
	ds_read2_b32 v[12:13], v77 offset0:66 offset1:74
	ds_read2_b32 v[14:15], v77 offset0:99 offset1:107
	ds_read2_b32 v[16:17], v77 offset0:132 offset1:140
	s_waitcnt lgkmcnt(4)
	v_bfe_u32 v2, v6, 16, 1
	s_waitcnt lgkmcnt(3)
	v_bfe_u32 v3, v8, 16, 1
	v_add3_u32 v2, v6, v2, s50
	v_lshrrev_b32_e32 v2, 16, v2
	v_add3_u32 v3, v8, v3, s50
	ds_read2_b32 v[18:19], v77 offset0:165 offset1:173
	v_and_or_b32 v2, v3, s51, v2
	s_waitcnt lgkmcnt(3)
	v_bfe_u32 v3, v12, 16, 1
	v_add3_u32 v3, v12, v3, s50
	s_waitcnt lgkmcnt(2)
	v_bfe_u32 v4, v14, 16, 1
	ds_read2_b32 v[20:21], v77 offset0:198 offset1:206
	v_lshrrev_b32_e32 v3, 16, v3
	v_add3_u32 v4, v14, v4, s50
	ds_read2_b32 v[22:23], v77 offset0:231 offset1:239
	v_and_or_b32 v3, v4, s51, v3
	s_waitcnt lgkmcnt(3)
	v_bfe_u32 v4, v16, 16, 1
	v_add3_u32 v4, v16, v4, s50
	s_waitcnt lgkmcnt(2)
	v_bfe_u32 v5, v18, 16, 1
	v_lshrrev_b32_e32 v4, 16, v4
	v_add3_u32 v5, v18, v5, s50
	v_and_or_b32 v4, v5, s51, v4
	s_waitcnt lgkmcnt(1)
	v_bfe_u32 v5, v20, 16, 1
	v_add3_u32 v5, v20, v5, s50
	s_waitcnt lgkmcnt(0)
	v_bfe_u32 v6, v22, 16, 1
	v_lshl_add_u64 v[10:11], s[0:1], 0, v[80:81]
	v_lshrrev_b32_e32 v5, 16, v5
	v_add3_u32 v6, v22, v6, s50
	v_and_or_b32 v5, v6, s51, v5
	v_mad_u64_u32 v[24:25], s[36:37], v66, s40, v[10:11]
	global_store_dwordx4 v[24:25], v[2:5], off sc1
	v_bfe_u32 v6, v23, 16, 1
	v_add3_u32 v6, v23, v6, s50
	v_bfe_u32 v2, v7, 16, 1
	v_add3_u32 v2, v7, v2, s50
	v_bfe_u32 v3, v9, 16, 1
	v_lshrrev_b32_e32 v2, 16, v2
	v_add3_u32 v3, v9, v3, s50
	v_and_or_b32 v2, v3, s51, v2
	v_bfe_u32 v3, v13, 16, 1
	v_add3_u32 v3, v13, v3, s50
	v_bfe_u32 v4, v15, 16, 1
	v_lshrrev_b32_e32 v3, 16, v3
	v_add3_u32 v4, v15, v4, s50
	v_and_or_b32 v3, v4, s51, v3
	v_bfe_u32 v4, v17, 16, 1
	v_add3_u32 v4, v17, v4, s50
	v_bfe_u32 v5, v19, 16, 1
	v_lshrrev_b32_e32 v4, 16, v4
	v_add3_u32 v5, v19, v5, s50
	v_and_or_b32 v4, v5, s51, v4
	v_bfe_u32 v5, v21, 16, 1
	v_add3_u32 v5, v21, v5, s50
	v_lshrrev_b32_e32 v5, 16, v5
	v_and_or_b32 v5, v6, s51, v5
	ds_read2_b32 v[6:7], v77 offset0:16 offset1:24
	v_mad_u64_u32 v[8:9], s[36:37], v72, s40, v[10:11]
	global_store_dwordx4 v[8:9], v[2:5], off sc1
	ds_read2_b32 v[8:9], v77 offset0:49 offset1:57
	ds_read2_b32 v[12:13], v77 offset0:82 offset1:90
	ds_read2_b32 v[14:15], v77 offset0:115 offset1:123
	s_waitcnt lgkmcnt(3)
	v_bfe_u32 v2, v6, 16, 1
	v_add3_u32 v2, v6, v2, s50
	s_waitcnt lgkmcnt(2)
	v_bfe_u32 v3, v8, 16, 1
	ds_read2_b32 v[16:17], v77 offset0:148 offset1:156
	v_lshrrev_b32_e32 v2, 16, v2
	v_add3_u32 v3, v8, v3, s50
	ds_read2_b32 v[18:19], v77 offset0:181 offset1:189
	v_and_or_b32 v2, v3, s51, v2
	s_waitcnt lgkmcnt(3)
	v_bfe_u32 v3, v12, 16, 1
	v_add3_u32 v3, v12, v3, s50
	s_waitcnt lgkmcnt(2)
	v_bfe_u32 v4, v14, 16, 1
	ds_read2_b32 v[20:21], v77 offset0:214 offset1:222
	v_lshrrev_b32_e32 v3, 16, v3
	v_add3_u32 v4, v14, v4, s50
	ds_read2_b32 v[22:23], v77 offset0:247 offset1:255
	v_and_or_b32 v3, v4, s51, v3
	s_waitcnt lgkmcnt(3)
	v_bfe_u32 v4, v16, 16, 1
	v_add3_u32 v4, v16, v4, s50
	s_waitcnt lgkmcnt(2)
	v_bfe_u32 v5, v18, 16, 1
	v_lshrrev_b32_e32 v4, 16, v4
	v_add3_u32 v5, v18, v5, s50
	v_and_or_b32 v4, v5, s51, v4
	s_waitcnt lgkmcnt(1)
	v_bfe_u32 v5, v20, 16, 1
	v_add3_u32 v5, v20, v5, s50
	s_waitcnt lgkmcnt(0)
	v_bfe_u32 v6, v22, 16, 1
	v_lshrrev_b32_e32 v5, 16, v5
	v_add3_u32 v6, v22, v6, s50
	v_and_or_b32 v5, v6, s51, v5
	v_mad_u64_u32 v[10:11], s[36:37], v74, s40, v[10:11]
	global_store_dwordx4 v[10:11], v[2:5], off sc1
	v_bfe_u32 v6, v23, 16, 1
	v_add3_u32 v6, v23, v6, s50
	v_bfe_u32 v2, v7, 16, 1
	v_add3_u32 v2, v7, v2, s50
	v_bfe_u32 v3, v9, 16, 1
	v_lshrrev_b32_e32 v2, 16, v2
	v_add3_u32 v3, v9, v3, s50
	v_and_or_b32 v2, v3, s51, v2
	v_bfe_u32 v3, v13, 16, 1
	v_add3_u32 v3, v13, v3, s50
	v_bfe_u32 v4, v15, 16, 1
	v_lshrrev_b32_e32 v3, 16, v3
	v_add3_u32 v4, v15, v4, s50
	v_and_or_b32 v3, v4, s51, v3
	v_bfe_u32 v4, v17, 16, 1
	v_add3_u32 v4, v17, v4, s50
	v_bfe_u32 v5, v19, 16, 1
	v_lshrrev_b32_e32 v4, 16, v4
	v_add3_u32 v5, v19, v5, s50
	v_and_or_b32 v4, v5, s51, v4
	v_bfe_u32 v5, v21, 16, 1
	v_add3_u32 v5, v21, v5, s50
	v_lshrrev_b32_e32 v5, 16, v5
	v_and_or_b32 v5, v6, s51, v5
	v_mov_b64_e32 v[6:7], v[76:77]
	v_mov_b64_e32 v[8:9], v[80:81]
.LBB0_60:
	v_lshl_add_u64 v[8:9], s[0:1], 0, v[8:9]
	v_mad_u64_u32 v[6:7], s[0:1], s40, v6, v[8:9]
	global_store_dwordx4 v[6:7], v[2:5], off sc1
	s_waitcnt lgkmcnt(0)
	s_cmp_gt_i32 s68, 0xdfff
	s_mov_b64 s[36:37], -1
	s_cbranch_scc1 .LBB0_30
	s_add_i32 s0, s47, s71
	s_cmp_lt_i32 s0, 0xe000
	s_cselect_b32 s29, s0, s6
	s_cmp_gt_i32 s29, 0x9fff
	s_mov_b64 s[38:39], -1
	s_cbranch_scc0 .LBB0_70
	s_cmpk_gt_u32 s29, 0xafff
	s_cbranch_scc0 .LBB0_67
	s_lshl_b32 s0, s29, 4
	s_and_b32 s70, s29, 1
	s_and_b32 s41, s0, 0xfe0
	s_cmpk_gt_u32 s29, 0xbfff
	s_mul_i32 s40, s41, 0x1080
	s_cbranch_scc0 .LBB0_65
	s_add_i32 s0, s29, 0xffff4000
	s_lshr_b32 s0, s0, 7
	s_and_b32 s0, s0, 0x1fffffe
	s_or_b32 s0, s0, s70
	s_lshl_b32 s24, s0, 6
	s_lshl_b64 s[0:1], s[24:25], 14
	s_add_u32 s0, s22, s0
	s_addc_u32 s1, s23, s1
	s_lshl_b32 s36, s41, 2
	s_add_u32 s36, s0, s36
	s_addc_u32 s37, s1, 0
	s_add_u32 s0, s43, s40
	s_addc_u32 s1, s44, 0
	s_add_u32 s0, s0, s24
	s_addc_u32 s1, s1, 0
	s_mov_b64 s[38:39], 0

.LBB0_84:
	ds_read2_b32 v[40:41], v75 offset0:16 offset1:49
	v_lshl_add_u64 v[42:43], s[26:27], 0, v[78:79]
	v_mad_u64_u32 v[42:43], s[34:35], s28, v82, v[42:43]
	s_andn2_b64 vcc, exec, s[30:31]
	s_waitcnt lgkmcnt(0)
	v_mul_f32_e32 v40, s69, v40
	v_mul_f32_e32 v39, s69, v41
	s_mov_b64 s[30:31], -1
	global_store_dwordx4 v[42:43], v[34:37], off sc1
	s_cbranch_vccnz .LBB0_86
	ds_read2_b32 v[36:37], v75 offset0:82 offset1:115
	ds_read2_b32 v[42:43], v75 offset0:148 offset1:181
	v_mov_b32_e32 v34, v71
	v_mov_b32_e32 v35, v71
	v_cvt_pk_fp8_f32 v34, v40, v39
	s_waitcnt lgkmcnt(1)
	v_mul_f32_e32 v41, s69, v36
	v_mul_f32_e32 v44, s69, v37
	s_waitcnt lgkmcnt(0)
	v_mul_f32_e32 v42, s69, v42
	v_mul_f32_e32 v43, s69, v43
	ds_read2_b32 v[36:37], v75 offset0:214 offset1:247
	v_cvt_pk_fp8_f32 v35, v42, v43
	ds_read2_b32 v[42:43], v38 offset0:24 offset1:57
	v_cvt_pk_fp8_f32 v34, v41, v44 op_sel:[0,0,1]
	ds_read2_b32 v[44:45], v38 offset0:90 offset1:123
	s_waitcnt lgkmcnt(2)
	v_mul_f32_e32 v36, s69, v36
	v_mul_f32_e32 v37, s69, v37
	v_cvt_pk_fp8_f32 v35, v36, v37 op_sel:[0,0,1]
	s_waitcnt lgkmcnt(1)
	v_mul_f32_e32 v37, s69, v42
	v_mul_f32_e32 v41, s69, v43
	ds_read2_b32 v[42:43], v38 offset0:156 offset1:189
	v_mov_b32_e32 v36, v71
	v_cvt_pk_fp8_f32 v36, v37, v41
	s_waitcnt lgkmcnt(1)
	v_mul_f32_e32 v41, s69, v44
	v_mul_f32_e32 v46, s69, v45
	ds_read2_b32 v[44:45], v38 offset0:222 offset1:255
	s_waitcnt lgkmcnt(1)
	v_mul_f32_e32 v42, s69, v42
	v_mul_f32_e32 v43, s69, v43
	v_mov_b32_e32 v37, v71
	v_cvt_pk_fp8_f32 v37, v42, v43
	v_cvt_pk_fp8_f32 v36, v41, v46 op_sel:[0,0,1]
	s_waitcnt lgkmcnt(0)
	v_mul_f32_e32 v41, s69, v44
	v_mul_f32_e32 v42, s69, v45
	v_cvt_pk_fp8_f32 v37, v41, v42 op_sel:[0,0,1]
	s_mov_b64 s[30:31], 0

.LBB0_89:
	s_and_b64 vcc, exec, s[34:35]
	v_mov_b64_e32 v[38:39], v[84:85]
	v_mov_b64_e32 v[40:41], v[78:79]
	s_cbranch_vccz .LBB0_29
	ds_read2_b32 v[38:39], v77 offset1:8
	ds_read2_b32 v[40:41], v77 offset0:33 offset1:41
	ds_read2_b32 v[44:45], v77 offset0:66 offset1:74
	ds_read2_b32 v[46:47], v77 offset0:99 offset1:107
	ds_read2_b32 v[48:49], v77 offset0:132 offset1:140
	s_waitcnt lgkmcnt(4)
	v_bfe_u32 v34, v38, 16, 1
	s_waitcnt lgkmcnt(3)
	v_bfe_u32 v35, v40, 16, 1
	v_add3_u32 v34, v38, v34, s50
	v_lshrrev_b32_e32 v34, 16, v34
	v_add3_u32 v35, v40, v35, s50
	ds_read2_b32 v[50:51], v77 offset0:165 offset1:173
	v_and_or_b32 v34, v35, s51, v34
	s_waitcnt lgkmcnt(3)
	v_bfe_u32 v35, v44, 16, 1
	v_add3_u32 v35, v44, v35, s50
	s_waitcnt lgkmcnt(2)
	v_bfe_u32 v36, v46, 16, 1
	ds_read2_b32 v[52:53], v77 offset0:198 offset1:206
	v_lshrrev_b32_e32 v35, 16, v35
	v_add3_u32 v36, v46, v36, s50
	ds_read2_b32 v[54:55], v77 offset0:231 offset1:239
	v_and_or_b32 v35, v36, s51, v35
	s_waitcnt lgkmcnt(3)
	v_bfe_u32 v36, v48, 16, 1
	v_add3_u32 v36, v48, v36, s50
	s_waitcnt lgkmcnt(2)
	v_bfe_u32 v37, v50, 16, 1
	v_lshrrev_b32_e32 v36, 16, v36
	v_add3_u32 v37, v50, v37, s50
	v_and_or_b32 v36, v37, s51, v36
	s_waitcnt lgkmcnt(1)
	v_bfe_u32 v37, v52, 16, 1
	v_add3_u32 v37, v52, v37, s50
	s_waitcnt lgkmcnt(0)
	v_bfe_u32 v38, v54, 16, 1
	v_lshl_add_u64 v[42:43], s[26:27], 0, v[80:81]
	v_lshrrev_b32_e32 v37, 16, v37
	v_add3_u32 v38, v54, v38, s50
	v_and_or_b32 v37, v38, s51, v37
	v_mad_u64_u32 v[56:57], s[30:31], s28, v66, v[42:43]
	global_store_dwordx4 v[56:57], v[34:37], off sc1
	v_bfe_u32 v38, v55, 16, 1
	v_add3_u32 v38, v55, v38, s50
	v_bfe_u32 v34, v39, 16, 1
	v_add3_u32 v34, v39, v34, s50
	v_bfe_u32 v35, v41, 16, 1
	v_lshrrev_b32_e32 v34, 16, v34
	v_add3_u32 v35, v41, v35, s50
	v_and_or_b32 v34, v35, s51, v34
	v_bfe_u32 v35, v45, 16, 1
	v_add3_u32 v35, v45, v35, s50
	v_bfe_u32 v36, v47, 16, 1
	v_lshrrev_b32_e32 v35, 16, v35
	v_add3_u32 v36, v47, v36, s50
	v_and_or_b32 v35, v36, s51, v35
	v_bfe_u32 v36, v49, 16, 1
	v_add3_u32 v36, v49, v36, s50
	v_bfe_u32 v37, v51, 16, 1
	v_lshrrev_b32_e32 v36, 16, v36
	v_add3_u32 v37, v51, v37, s50
	v_and_or_b32 v36, v37, s51, v36
	v_bfe_u32 v37, v53, 16, 1
	v_add3_u32 v37, v53, v37, s50
	v_lshrrev_b32_e32 v37, 16, v37
	v_and_or_b32 v37, v38, s51, v37
	ds_read2_b32 v[38:39], v77 offset0:16 offset1:24
	v_mad_u64_u32 v[40:41], s[30:31], s28, v72, v[42:43]
	global_store_dwordx4 v[40:41], v[34:37], off sc1
	ds_read2_b32 v[40:41], v77 offset0:49 offset1:57
	ds_read2_b32 v[44:45], v77 offset0:82 offset1:90
	ds_read2_b32 v[46:47], v77 offset0:115 offset1:123
	s_waitcnt lgkmcnt(3)
	v_bfe_u32 v34, v38, 16, 1
	v_add3_u32 v34, v38, v34, s50
	s_waitcnt lgkmcnt(2)
	v_bfe_u32 v35, v40, 16, 1
	ds_read2_b32 v[48:49], v77 offset0:148 offset1:156
	v_lshrrev_b32_e32 v34, 16, v34
	v_add3_u32 v35, v40, v35, s50
	ds_read2_b32 v[50:51], v77 offset0:181 offset1:189
	v_and_or_b32 v34, v35, s51, v34
	s_waitcnt lgkmcnt(3)
	v_bfe_u32 v35, v44, 16, 1
	v_add3_u32 v35, v44, v35, s50
	s_waitcnt lgkmcnt(2)
	v_bfe_u32 v36, v46, 16, 1
	ds_read2_b32 v[52:53], v77 offset0:214 offset1:222
	v_lshrrev_b32_e32 v35, 16, v35
	v_add3_u32 v36, v46, v36, s50
	ds_read2_b32 v[54:55], v77 offset0:247 offset1:255
	v_and_or_b32 v35, v36, s51, v35
	s_waitcnt lgkmcnt(3)
	v_bfe_u32 v36, v48, 16, 1
	v_add3_u32 v36, v48, v36, s50
	s_waitcnt lgkmcnt(2)
	v_bfe_u32 v37, v50, 16, 1
	v_lshrrev_b32_e32 v36, 16, v36
	v_add3_u32 v37, v50, v37, s50
	v_and_or_b32 v36, v37, s51, v36
	s_waitcnt lgkmcnt(1)
	v_bfe_u32 v37, v52, 16, 1
	v_add3_u32 v37, v52, v37, s50
	s_waitcnt lgkmcnt(0)
	v_bfe_u32 v38, v54, 16, 1
	v_lshrrev_b32_e32 v37, 16, v37
	v_add3_u32 v38, v54, v38, s50
	v_and_or_b32 v37, v38, s51, v37
	v_mad_u64_u32 v[42:43], s[30:31], s28, v74, v[42:43]
	global_store_dwordx4 v[42:43], v[34:37], off sc1
	v_bfe_u32 v38, v55, 16, 1
	v_add3_u32 v38, v55, v38, s50
	v_bfe_u32 v34, v39, 16, 1
	v_add3_u32 v34, v39, v34, s50
	v_bfe_u32 v35, v41, 16, 1
	v_lshrrev_b32_e32 v34, 16, v34
	v_add3_u32 v35, v41, v35, s50
	v_and_or_b32 v34, v35, s51, v34
	v_bfe_u32 v35, v45, 16, 1
	v_add3_u32 v35, v45, v35, s50
	v_bfe_u32 v36, v47, 16, 1
	v_lshrrev_b32_e32 v35, 16, v35
	v_add3_u32 v36, v47, v36, s50
	v_and_or_b32 v35, v36, s51, v35
	v_bfe_u32 v36, v49, 16, 1
	v_add3_u32 v36, v49, v36, s50
	v_bfe_u32 v37, v51, 16, 1
	v_lshrrev_b32_e32 v36, 16, v36
	v_add3_u32 v37, v51, v37, s50
	v_and_or_b32 v36, v37, s51, v36
	v_bfe_u32 v37, v53, 16, 1
	v_add3_u32 v37, v53, v37, s50
	v_lshrrev_b32_e32 v37, 16, v37
	v_and_or_b32 v37, v38, s51, v37
	v_mov_b64_e32 v[38:39], v[76:77]
	v_mov_b64_e32 v[40:41], v[80:81]
	s_branch .LBB0_29
